# v069 + instruction selection: score-accumulator init in the attention loops uses 1 v_mov_b32 + 7 v_mov_b64 instead of 15 v_mov_b32
# baseline (speedup 1.0000x reference)
; #define LAS __attribute__((address_space(3)))
; #define MFMA32(a, b, c) __builtin_amdgcn_mfma_f32_32x32x16_bf16((a), (b), (c), 0, 0, 0)
;     __device__ __forceinline__ void init(const void* A_, const void* B_, int lda_, int ldb_, int M, unsigned mask_, int G_, int c_) { A = (const char*)A_; B = (const char*)B_; lda = lda_; ldb = ldb_; nM = M / BM; mask = mask_; nN = __builtin_popcount(mask_); nwg = nM * nN; G = G_; c = c_; }
;     __device__ __forceinline__ void init(f32x4 (&acc)[2][2][4][2], const Unit& u, int wr, int wc, int fr, int fq) const { u32x4 old[2][4][2]; init_load(old, u, wr, wc, fr, fq); init_finish(acc, old); }
; template <int KS> DI void at_qk(f32x16& p0, f32x16& p1, LAS const unsigned char* Kt, int mapB, const bf16x8 (&qr)[8], float init, int r32, int hi) {
; #pragma unroll
;     for (int i = 0; i < 16; ++i) { p0[i] = init; p1[i] = init; }
;     bf16x8 kb[KS][2];
; #pragma unroll
;     for (int d0 = 0; d0 < KS; ++d0) { const int cb = mapB + (d0 * 16 + hi * 8) * 2;
;         kb[d0][0] = *(const LAS bf16x8*)(Kt + AT_KSWZ(r32, cb)); kb[d0][1] = *(const LAS bf16x8*)(Kt + AT_KSWZ(32 + r32, cb)); }
;     __builtin_amdgcn_sched_barrier(0);
; #pragma unroll
;     for (int d0 = 0; d0 < KS; ++d0) { p0 = MFMA32(kb[d0][0], qr[d0], p0); p1 = MFMA32(kb[d0][1], qr[d0], p1); }
; }
; DI float at_softmax(f32x16& p0, f32x16& p1, float& m_run, bool first, bool nearb, LAS const float* tabp, int lane) {
;     if (nearb) {
; #pragma unroll
;         for (int i = 0; i < 16; ++i) { p0[i] += tabp[8 * (i >> 2) + (i & 3)]; p1[i] += tabp[32 + 8 * (i >> 2) + (i & 3)]; }
.LBB0_792:
	s_mul_hi_u32 s57, s94, 0xaaaaaaab
	s_lshr_b32 s57, s57, 1
	s_mul_i32 s57, s57, 0x18000
	s_cmp_le_u32 s48, s88
	v_subrev_u32_e32 v0, s57, v161
	s_cselect_b64 vcc, -1, 0
	s_add_i32 s58, s49, 0
	v_subrev_u32_e32 v10, s57, v162
	s_waitcnt lgkmcnt(0)
	v_cndmask_b32_e32 v2, 0, v158, vcc
	v_add_u32_e32 v0, s58, v0
	v_subrev_u32_e32 v14, s57, v163
	v_sub_f32_e32 v96, v2, v165
	ds_read_b128 v[2:5], v0
	ds_read_b128 v[6:9], v0 offset:8192
	v_add_u32_e32 v0, s58, v10
	v_subrev_u32_e32 v15, s57, v164
	ds_read_b128 v[10:13], v0
	ds_read_b128 v[166:169], v0 offset:8192
	v_add_u32_e32 v0, s58, v14
	ds_read_b128 v[170:173], v0
	ds_read_b128 v[174:177], v0 offset:8192
	v_add_u32_e32 v0, s58, v15
	ds_read_b128 v[178:181], v0
	ds_read_b128 v[182:185], v0 offset:8192
	v_mov_b32_e32 v97, v96
	v_mov_b64_e32 v[98:99], v[96:97]
	v_mov_b64_e32 v[100:101], v[96:97]
	v_mov_b64_e32 v[102:103], v[96:97]
	v_mov_b64_e32 v[104:105], v[96:97]
	v_mov_b64_e32 v[106:107], v[96:97]
	v_mov_b64_e32 v[108:109], v[96:97]
	v_mov_b64_e32 v[110:111], v[96:97]
	s_waitcnt lgkmcnt(0)
	s_nop 0
	v_mfma_f32_32x32x16_bf16 v[112:127], v[2:5], v[128:131], v[96:111]
	s_and_b64 vcc, exec, vcc
	v_mfma_f32_32x32x16_bf16 v[96:111], v[6:9], v[128:131], v[96:111]
	v_mfma_f32_32x32x16_bf16 v[112:127], v[10:13], v[132:135], v[112:127]
	v_mfma_f32_32x32x16_bf16 v[96:111], v[166:169], v[132:135], v[96:111]
	v_mfma_f32_32x32x16_bf16 v[112:127], v[170:173], v[136:139], v[112:127]
	v_mfma_f32_32x32x16_bf16 v[96:111], v[174:177], v[136:139], v[96:111]
	v_mfma_f32_32x32x16_bf16 v[112:127], v[178:181], v[140:143], v[112:127]
	v_mfma_f32_32x32x16_bf16 v[96:111], v[182:185], v[140:143], v[96:111]
	s_cbranch_vccnz .LBB0_794
	v_add_u32_e32 v0, 0, v159
	v_add_u32_e32 v2, 0x207fc, v0
	v_add_u32_e32 v4, 0x2087c, v0
	ds_read2_b32 v[2:3], v2 offset1:1
	ds_read2_b32 v[4:5], v4 offset1:1
	v_add_u32_e32 v6, 0x20804, v0
	v_add_u32_e32 v8, 0x20884, v0
	v_add_u32_e32 v10, 0x2081c, v0
	v_add_u32_e32 v12, 0x2089c, v0
	v_add_u32_e32 v14, 0x20824, v0
	v_add_u32_e32 v166, 0x208a4, v0
	v_add_u32_e32 v168, 0x2083c, v0
	v_add_u32_e32 v170, 0x208bc, v0
	v_add_u32_e32 v172, 0x20844, v0
	v_add_u32_e32 v174, 0x208c4, v0
	v_add_u32_e32 v176, 0x2085c, v0
	v_add_u32_e32 v178, 0x208dc, v0
	v_add_u32_e32 v180, 0x20864, v0
	v_add_u32_e32 v0, 0x208e4, v0
	ds_read2_b32 v[6:7], v6 offset1:1
	ds_read2_b32 v[8:9], v8 offset1:1
	ds_read2_b32 v[10:11], v10 offset1:1
	ds_read2_b32 v[12:13], v12 offset1:1
	ds_read2_b32 v[14:15], v14 offset1:1
	ds_read2_b32 v[166:167], v166 offset1:1
	ds_read2_b32 v[168:169], v168 offset1:1
	ds_read2_b32 v[170:171], v170 offset1:1
	ds_read2_b32 v[172:173], v172 offset1:1
	ds_read2_b32 v[174:175], v174 offset1:1
	ds_read2_b32 v[176:177], v176 offset1:1
	ds_read2_b32 v[178:179], v178 offset1:1
	ds_read2_b32 v[180:181], v180 offset1:1
	s_waitcnt lgkmcnt(0)
	v_pk_add_f32 v[112:113], v[112:113], v[2:3]
	ds_read2_b32 v[2:3], v0 offset1:1
	v_pk_add_f32 v[124:125], v[124:125], v[176:177]
	v_pk_add_f32 v[122:123], v[122:123], v[172:173]
	v_pk_add_f32 v[126:127], v[126:127], v[180:181]
	v_pk_add_f32 v[120:121], v[120:121], v[168:169]
	v_pk_add_f32 v[118:119], v[118:119], v[14:15]
	v_pk_add_f32 v[116:117], v[116:117], v[10:11]
	v_pk_add_f32 v[114:115], v[114:115], v[6:7]
	s_waitcnt lgkmcnt(0)
	v_pk_add_f32 v[110:111], v[110:111], v[2:3]
	v_pk_add_f32 v[108:109], v[108:109], v[178:179]
	v_pk_add_f32 v[106:107], v[106:107], v[174:175]
	v_pk_add_f32 v[104:105], v[104:105], v[170:171]
	v_pk_add_f32 v[102:103], v[102:103], v[166:167]
	v_pk_add_f32 v[100:101], v[100:101], v[12:13]
	v_pk_add_f32 v[98:99], v[98:99], v[8:9]
	v_pk_add_f32 v[96:97], v[96:97], v[4:5]

; #define LAS __attribute__((address_space(3)))
; #define MFMA32(a, b, c) __builtin_amdgcn_mfma_f32_32x32x16_bf16((a), (b), (c), 0, 0, 0)
;     __device__ __forceinline__ void init(const void* A_, const void* B_, int lda_, int ldb_, int M, unsigned mask_, int G_, int c_) { A = (const char*)A_; B = (const char*)B_; lda = lda_; ldb = ldb_; nM = M / BM; mask = mask_; nN = __builtin_popcount(mask_); nwg = nM * nN; G = G_; c = c_; }
;     __device__ __forceinline__ void init(f32x4 (&acc)[2][2][4][2], const Unit& u, int wr, int wc, int fr, int fq) const { u32x4 old[2][4][2]; init_load(old, u, wr, wc, fr, fq); init_finish(acc, old); }
; template <int KS> DI void at_qk(f32x16& p0, f32x16& p1, LAS const unsigned char* Kt, int mapB, const bf16x8 (&qr)[8], float init, int r32, int hi) {
; #pragma unroll
;     for (int i = 0; i < 16; ++i) { p0[i] = init; p1[i] = init; }
;     bf16x8 kb[KS][2];
; #pragma unroll
;     for (int d0 = 0; d0 < KS; ++d0) { const int cb = mapB + (d0 * 16 + hi * 8) * 2;
;         kb[d0][0] = *(const LAS bf16x8*)(Kt + AT_KSWZ(r32, cb)); kb[d0][1] = *(const LAS bf16x8*)(Kt + AT_KSWZ(32 + r32, cb)); }
;     __builtin_amdgcn_sched_barrier(0);
; #pragma unroll
;     for (int d0 = 0; d0 < KS; ++d0) { p0 = MFMA32(kb[d0][0], qr[d0], p0); p1 = MFMA32(kb[d0][1], qr[d0], p1); }
; }
; DI float at_softmax(f32x16& p0, f32x16& p1, float& m_run, bool first, bool nearb, LAS const float* tabp, int lane) {
;     if (nearb) {
; #pragma unroll
;         for (int i = 0; i < 16; ++i) { p0[i] += tabp[8 * (i >> 2) + (i & 3)]; p1[i] += tabp[32 + 8 * (i >> 2) + (i & 3)]; }
.LBB0_835:
	s_mul_hi_u32 s48, s35, 0xaaaaaaab
	s_lshr_b32 s48, s48, 1
	s_mul_i32 s48, s48, 0x18000
	s_cmp_le_i32 s28, s16
	v_subrev_u32_e32 v0, s48, v161
	s_cselect_b64 vcc, -1, 0
	s_add_i32 s49, s31, 0
	v_subrev_u32_e32 v10, s48, v162
	s_waitcnt lgkmcnt(0)
	v_cndmask_b32_e32 v2, 0, v158, vcc
	v_add_u32_e32 v0, s49, v0
	v_subrev_u32_e32 v14, s48, v163
	v_sub_f32_e32 v96, v2, v165
	ds_read_b128 v[2:5], v0
	ds_read_b128 v[6:9], v0 offset:8192
	v_add_u32_e32 v0, s49, v10
	v_subrev_u32_e32 v15, s48, v164
	ds_read_b128 v[10:13], v0
	ds_read_b128 v[166:169], v0 offset:8192
	v_add_u32_e32 v0, s49, v14
	ds_read_b128 v[170:173], v0
	ds_read_b128 v[174:177], v0 offset:8192
	v_add_u32_e32 v0, s49, v15
	ds_read_b128 v[178:181], v0
	ds_read_b128 v[182:185], v0 offset:8192
	v_mov_b32_e32 v97, v96
	v_mov_b64_e32 v[98:99], v[96:97]
	v_mov_b64_e32 v[100:101], v[96:97]
	v_mov_b64_e32 v[102:103], v[96:97]
	v_mov_b64_e32 v[104:105], v[96:97]
	v_mov_b64_e32 v[106:107], v[96:97]
	v_mov_b64_e32 v[108:109], v[96:97]
	v_mov_b64_e32 v[110:111], v[96:97]
	s_waitcnt lgkmcnt(0)
	s_nop 0
	v_mfma_f32_32x32x16_bf16 v[112:127], v[2:5], v[128:131], v[96:111]
	s_and_b64 vcc, exec, vcc
	v_mfma_f32_32x32x16_bf16 v[96:111], v[6:9], v[128:131], v[96:111]
	v_mfma_f32_32x32x16_bf16 v[112:127], v[10:13], v[132:135], v[112:127]
	v_mfma_f32_32x32x16_bf16 v[96:111], v[166:169], v[132:135], v[96:111]
	v_mfma_f32_32x32x16_bf16 v[112:127], v[170:173], v[136:139], v[112:127]
	v_mfma_f32_32x32x16_bf16 v[96:111], v[174:177], v[136:139], v[96:111]
	v_mfma_f32_32x32x16_bf16 v[112:127], v[178:181], v[140:143], v[112:127]
	v_mfma_f32_32x32x16_bf16 v[96:111], v[182:185], v[140:143], v[96:111]
	s_cbranch_vccnz .LBB0_837
	v_add_u32_e32 v0, 0, v159
	v_add_u32_e32 v2, 0x207fc, v0
	v_add_u32_e32 v4, 0x2087c, v0
	ds_read2_b32 v[2:3], v2 offset1:1
	ds_read2_b32 v[4:5], v4 offset1:1
	v_add_u32_e32 v6, 0x20804, v0
	v_add_u32_e32 v8, 0x20884, v0
	v_add_u32_e32 v10, 0x2081c, v0
	v_add_u32_e32 v12, 0x2089c, v0
	v_add_u32_e32 v14, 0x20824, v0
	v_add_u32_e32 v166, 0x208a4, v0
	v_add_u32_e32 v168, 0x2083c, v0
	v_add_u32_e32 v170, 0x208bc, v0
	v_add_u32_e32 v172, 0x20844, v0
	v_add_u32_e32 v174, 0x208c4, v0
	v_add_u32_e32 v176, 0x2085c, v0
	v_add_u32_e32 v178, 0x208dc, v0
	v_add_u32_e32 v180, 0x20864, v0
	v_add_u32_e32 v0, 0x208e4, v0
	ds_read2_b32 v[6:7], v6 offset1:1
	ds_read2_b32 v[8:9], v8 offset1:1
	ds_read2_b32 v[10:11], v10 offset1:1
	ds_read2_b32 v[12:13], v12 offset1:1
	ds_read2_b32 v[14:15], v14 offset1:1
	ds_read2_b32 v[166:167], v166 offset1:1
	ds_read2_b32 v[168:169], v168 offset1:1
	ds_read2_b32 v[170:171], v170 offset1:1
	ds_read2_b32 v[172:173], v172 offset1:1
	ds_read2_b32 v[174:175], v174 offset1:1
	ds_read2_b32 v[176:177], v176 offset1:1
	ds_read2_b32 v[178:179], v178 offset1:1
	ds_read2_b32 v[180:181], v180 offset1:1
	s_waitcnt lgkmcnt(0)
	v_pk_add_f32 v[112:113], v[112:113], v[2:3]
	ds_read2_b32 v[2:3], v0 offset1:1
	v_pk_add_f32 v[124:125], v[124:125], v[176:177]
	v_pk_add_f32 v[122:123], v[122:123], v[172:173]
	v_pk_add_f32 v[126:127], v[126:127], v[180:181]
	v_pk_add_f32 v[120:121], v[120:121], v[168:169]
	v_pk_add_f32 v[118:119], v[118:119], v[14:15]
	v_pk_add_f32 v[116:117], v[116:117], v[10:11]
	v_pk_add_f32 v[114:115], v[114:115], v[6:7]
	s_waitcnt lgkmcnt(0)
	v_pk_add_f32 v[110:111], v[110:111], v[2:3]
	v_pk_add_f32 v[108:109], v[108:109], v[178:179]
	v_pk_add_f32 v[106:107], v[106:107], v[174:175]
	v_pk_add_f32 v[104:105], v[104:105], v[170:171]
	v_pk_add_f32 v[102:103], v[102:103], v[166:167]
	v_pk_add_f32 v[100:101], v[100:101], v[12:13]
	v_pk_add_f32 v[98:99], v[98:99], v[8:9]
	v_pk_add_f32 v[96:97], v[96:97], v[4:5]

; #define LAS __attribute__((address_space(3)))
; #define MFMA32(a, b, c) __builtin_amdgcn_mfma_f32_32x32x16_bf16((a), (b), (c), 0, 0, 0)
;     __device__ __forceinline__ void init(const void* A_, const void* B_, int lda_, int ldb_, int M, unsigned mask_, int G_, int c_) { A = (const char*)A_; B = (const char*)B_; lda = lda_; ldb = ldb_; nM = M / BM; mask = mask_; nN = __builtin_popcount(mask_); nwg = nM * nN; G = G_; c = c_; }
;     __device__ __forceinline__ void init(f32x4 (&acc)[2][2][4][2], const Unit& u, int wr, int wc, int fr, int fq) const { u32x4 old[2][4][2]; init_load(old, u, wr, wc, fr, fq); init_finish(acc, old); }
; template <int KS> DI void at_qk(f32x16& p0, f32x16& p1, LAS const unsigned char* Kt, int mapB, const bf16x8 (&qr)[8], float init, int r32, int hi) {
; #pragma unroll
;     for (int i = 0; i < 16; ++i) { p0[i] = init; p1[i] = init; }
;     bf16x8 kb[KS][2];
; #pragma unroll
;     for (int d0 = 0; d0 < KS; ++d0) { const int cb = mapB + (d0 * 16 + hi * 8) * 2;
;         kb[d0][0] = *(const LAS bf16x8*)(Kt + AT_KSWZ(r32, cb)); kb[d0][1] = *(const LAS bf16x8*)(Kt + AT_KSWZ(32 + r32, cb)); }
;     __builtin_amdgcn_sched_barrier(0);
; #pragma unroll
;     for (int d0 = 0; d0 < KS; ++d0) { p0 = MFMA32(kb[d0][0], qr[d0], p0); p1 = MFMA32(kb[d0][1], qr[d0], p1); }
; }
; DI float at_softmax(f32x16& p0, f32x16& p1, float& m_run, bool first, bool nearb, LAS const float* tabp, int lane) {
;     if (nearb) {
; #pragma unroll
;         for (int i = 0; i < 16; ++i) { p0[i] += tabp[8 * (i >> 2) + (i & 3)]; p1[i] += tabp[32 + 8 * (i >> 2) + (i & 3)]; }
; DI void attn_unit_band(const Ctx& C, int l, int b, int h, int qt) {
;     ...
;         if (kt <= cw && kt >= cw - 8) {
;             LAS const unsigned char* Kt = C.lds + slot * 32768;
;             const int vb = (int)(size_t)(Kt + 16384) + vrd;
;             const bool nearb = (kt * 64 + 63 - q0w) > -128;
;             LAS const float* tabp = tabl + (kt * 64 - qpos + TABA_OFF + 4 * hi);
;             f32x16 p0, p1;
;             at_qk<KS>(p0, p1, Kt, 0, qr, (nearb ? 0.f : cfar) - m_run, r32, hi);
;             const float alpha = at_softmax(p0, p1, m_run, first, nearb, tabp, lane);
.LBB0_880:
	s_mul_hi_u32 s48, s76, 0xaaaaaaab
	s_lshr_b32 s57, s48, 1
	s_mul_i32 s57, s57, 0x18000
	v_subrev_u32_e32 v108, s57, v157
	v_add_u32_e32 v116, s75, v168
	v_subrev_u32_e32 v109, s57, v158
	v_add_u32_e32 v108, v116, v108
	v_subrev_u32_e32 v110, s57, v159
	ds_read_b128 v[170:173], v108
	ds_read_b128 v[174:177], v108 offset:8192
	v_add_u32_e32 v108, v116, v109
	v_subrev_u32_e32 v111, s57, v160
	ds_read_b128 v[178:181], v108
	ds_read_b128 v[182:185], v108 offset:8192
	v_add_u32_e32 v108, v116, v110
	v_subrev_u32_e32 v112, s57, v161
	ds_read_b128 v[186:189], v108
	ds_read_b128 v[190:193], v108 offset:8192
	v_add_u32_e32 v108, v116, v111
	v_subrev_u32_e32 v113, s57, v162
	ds_read_b128 v[206:209], v108
	ds_read_b128 v[210:213], v108 offset:8192
	v_add_u32_e32 v108, v116, v112
	v_subrev_u32_e32 v114, s57, v163
	ds_read_b128 v[214:217], v108
	ds_read_b128 v[218:221], v108 offset:8192
	v_add_u32_e32 v108, v116, v113
	v_subrev_u32_e32 v115, s57, v164
	ds_read_b128 v[232:235], v108
	ds_read_b128 v[236:239], v108 offset:8192
	v_add_u32_e32 v108, v116, v114
	ds_read_b128 v[240:243], v108
	ds_read_b128 v[244:247], v108 offset:8192
	v_add_u32_e32 v108, v116, v115
	s_cmpk_lt_i32 s74, 0xff81
	ds_read_b128 v[202:205], v108
	ds_read_b128 v[222:225], v108 offset:8192
	s_cselect_b64 vcc, -1, 0
	v_cndmask_b32_e32 v96, 0, v149, vcc
	v_sub_f32_e32 v96, v96, v169
	v_mov_b32_e32 v97, v96
	v_mov_b64_e32 v[98:99], v[96:97]
	v_mov_b64_e32 v[100:101], v[96:97]
	v_mov_b64_e32 v[102:103], v[96:97]
	v_mov_b64_e32 v[104:105], v[96:97]
	v_mov_b64_e32 v[106:107], v[96:97]
	v_mov_b64_e32 v[108:109], v[96:97]
	v_mov_b64_e32 v[110:111], v[96:97]
	s_waitcnt lgkmcnt(0)
	s_nop 0
	v_mfma_f32_32x32x16_bf16 v[112:127], v[170:173], v[2:5], v[96:111]
	s_and_b64 vcc, exec, vcc
	v_mfma_f32_32x32x16_bf16 v[96:111], v[174:177], v[2:5], v[96:111]
	v_mfma_f32_32x32x16_bf16 v[112:127], v[178:181], v[6:9], v[112:127]
	v_mfma_f32_32x32x16_bf16 v[96:111], v[182:185], v[6:9], v[96:111]
	v_mfma_f32_32x32x16_bf16 v[112:127], v[186:189], v[10:13], v[112:127]
	v_mfma_f32_32x32x16_bf16 v[96:111], v[190:193], v[10:13], v[96:111]
	v_mfma_f32_32x32x16_bf16 v[112:127], v[206:209], v[128:131], v[112:127]
	v_mfma_f32_32x32x16_bf16 v[96:111], v[210:213], v[128:131], v[96:111]
	v_mfma_f32_32x32x16_bf16 v[112:127], v[214:217], v[132:135], v[112:127]
	v_mfma_f32_32x32x16_bf16 v[96:111], v[218:221], v[132:135], v[96:111]
	v_mfma_f32_32x32x16_bf16 v[112:127], v[232:235], v[136:139], v[112:127]
	v_mfma_f32_32x32x16_bf16 v[96:111], v[236:239], v[136:139], v[96:111]
	v_mfma_f32_32x32x16_bf16 v[112:127], v[240:243], v[140:143], v[112:127]
	v_mfma_f32_32x32x16_bf16 v[96:111], v[244:247], v[140:143], v[96:111]
	v_mfma_f32_32x32x16_bf16 v[112:127], v[202:205], v[144:147], v[112:127]
	v_mfma_f32_32x32x16_bf16 v[96:111], v[222:225], v[144:147], v[96:111]
	s_cbranch_vccnz .LBB0_882
	v_add_u32_e32 v152, 0, v166
	v_add_u32_e32 v170, 0x20400, v152
	v_add_u32_e32 v172, 0x20480, v152
	ds_read2_b32 v[170:171], v170 offset1:1
	ds_read2_b32 v[172:173], v172 offset1:1
	v_add_u32_e32 v174, 0x20408, v152
	v_add_u32_e32 v176, 0x20488, v152
	v_add_u32_e32 v178, 0x20420, v152
	v_add_u32_e32 v180, 0x204a0, v152
	v_add_u32_e32 v182, 0x20428, v152
	v_add_u32_e32 v184, 0x204a8, v152
	v_add_u32_e32 v186, 0x20440, v152
	v_add_u32_e32 v188, 0x204c0, v152
	v_add_u32_e32 v190, 0x20448, v152
	v_add_u32_e32 v192, 0x204c8, v152
	v_add_u32_e32 v197, 0x20460, v152
	v_add_u32_e32 v204, 0x204e0, v152
	ds_read2_b32 v[174:175], v174 offset1:1
	ds_read2_b32 v[176:177], v176 offset1:1
	ds_read2_b32 v[178:179], v178 offset1:1
	ds_read2_b32 v[180:181], v180 offset1:1
	ds_read2_b32 v[182:183], v182 offset1:1
	ds_read2_b32 v[184:185], v184 offset1:1
	ds_read2_b32 v[186:187], v186 offset1:1
	ds_read2_b32 v[188:189], v188 offset1:1
	ds_read2_b32 v[190:191], v190 offset1:1
	ds_read2_b32 v[192:193], v192 offset1:1
	ds_read2_b32 v[202:203], v197 offset1:1
	ds_read2_b32 v[204:205], v204 offset1:1
	v_add_u32_e32 v197, 0x20468, v152
	v_add_u32_e32 v152, 0x204e8, v152
	ds_read2_b32 v[206:207], v197 offset1:1
	s_waitcnt lgkmcnt(0)
	v_pk_add_f32 v[112:113], v[112:113], v[170:171]
	ds_read2_b32 v[170:171], v152 offset1:1
	v_pk_add_f32 v[124:125], v[124:125], v[202:203]
	v_pk_add_f32 v[122:123], v[122:123], v[190:191]
	v_pk_add_f32 v[126:127], v[126:127], v[206:207]
	v_pk_add_f32 v[120:121], v[120:121], v[186:187]
	v_pk_add_f32 v[118:119], v[118:119], v[182:183]
	v_pk_add_f32 v[116:117], v[116:117], v[178:179]
	v_pk_add_f32 v[114:115], v[114:115], v[174:175]
	s_waitcnt lgkmcnt(0)
	v_pk_add_f32 v[110:111], v[110:111], v[170:171]
	v_pk_add_f32 v[108:109], v[108:109], v[204:205]
	v_pk_add_f32 v[106:107], v[106:107], v[192:193]
	v_pk_add_f32 v[104:105], v[104:105], v[188:189]
	v_pk_add_f32 v[102:103], v[102:103], v[184:185]
	v_pk_add_f32 v[100:101], v[100:101], v[180:181]
	v_pk_add_f32 v[98:99], v[98:99], v[176:177]
	v_pk_add_f32 v[96:97], v[96:97], v[172:173]
